# mLSTM: second conversion slot (every third chunk) dropped - one tile per chunk for 32 chunks, uniform memory-pipe load
# baseline (speedup 1.0000x reference)
; __device__ __forceinline__ void mlstm_unit(LAS unsigned char* lds, const bf16_t* __restrict__ PM, const float* __restrict__ GATES, bf16_t* __restrict__ Hout,
;                                            int b, int h, int dir, int vs, Conv& cvs, const int wave_) {
;     ...
;         CV_FINISH();
;         if ((ci % 3) == 0) { CV_ISSUE(); pend_b = true; }
.LBB0_608:
	s_add_i32 s33, s33, s62
	s_mov_b64 s[30:31], 0
	s_cmp_lt_i32 s33, s101
	s_cselect_b64 s[2:3], -1, 0
	s_and_b64 s[2:3], s[30:31], s[2:3]
	s_andn2_b64 vcc, exec, s[2:3]
	s_cbranch_vccnz .LBB0_615
	s_cmp_gt_i32 s33, 0xffff
	s_mov_b64 s[2:3], -1
	s_cbranch_scc0 .LBB0_611
	s_add_i32 s0, s33, 0xffff0000
	s_lshr_b32 s2, s0, 10
	s_mov_b32 s3, s79
	v_readlane_b32 s36, v254, 34
	s_lshl_b64 s[2:3], s[2:3], 24
	v_readlane_b32 s44, v254, 42
	v_readlane_b32 s45, v254, 43
	s_add_u32 s72, s44, s2
	v_readlane_b32 s37, v254, 35
	v_readlane_b32 s38, v254, 36
	v_readlane_b32 s39, v254, 37
	v_readlane_b32 s40, v254, 38
	v_readlane_b32 s41, v254, 39
	v_readlane_b32 s42, v254, 40
	v_readlane_b32 s43, v254, 41
	v_readlane_b32 s46, v254, 44
	v_readlane_b32 s47, v254, 45
	v_readlane_b32 s48, v254, 46
	v_readlane_b32 s49, v254, 47
	v_readlane_b32 s50, v254, 48
	v_readlane_b32 s51, v254, 49
	s_addc_u32 s73, s45, s3
	s_lshl_b32 s0, s33, 1
	s_mov_b64 s[2:3], 0
